# baseline (speedup 1.0000x reference)
.LBB1_12:
	s_mov_b32 s0, s44
	s_add_i32 s44, s44, 1
	s_cmp_ge_u32 s44, s42
	s_cselect_b64 s[22:23], -1, 0
	s_cmp_lt_u32 s44, s42
	s_cselect_b32 s2, s44, s0
	s_waitcnt vmcnt(0)
	s_lshl_b32 s0, s2, 4
	s_mov_b32 s1, s17
	s_mov_b32 m0, s43
	ds_read_b128 v[76:79], v119 offset:32768
	ds_read_b128 v[80:83], v119 offset:36864
	ds_read_b128 v[84:87], v120 offset:32768
	ds_read_b128 v[88:91], v120 offset:36864
	ds_read_b128 v[92:95], v121
	ds_read_b128 v[96:99], v121 offset:4096
	ds_read_b128 v[128:131], v122
	ds_read_b128 v[132:135], v122 offset:4096
	ds_read_b128 v[72:75], v123
	s_waitcnt lgkmcnt(0)
	v_lshl_add_u64 v[70:71], s[0:1], 2, v[2:3]
	global_load_lds_dword v[70:71], off
	ds_read_b128 v[156:159], v115
	ds_read_b128 v[160:163], v115 offset:1024
	ds_read_b128 v[164:167], v115 offset:2048
	v_cvt_pk_bf16_f32 v136, v76, v77
	v_cvt_pk_bf16_f32 v137, v78, v79
	v_cvt_pk_bf16_f32 v138, v84, v85
	v_cvt_pk_bf16_f32 v139, v86, v87
	v_cvt_pk_bf16_f32 v140, v92, v93
	v_cvt_pk_bf16_f32 v141, v94, v95
	v_cvt_pk_bf16_f32 v142, v128, v129
	v_cvt_pk_bf16_f32 v143, v130, v131
	v_cvt_pk_bf16_f32 v144, v80, v81
	v_cvt_pk_bf16_f32 v145, v82, v83
	v_cvt_pk_bf16_f32 v146, v88, v89
	v_cvt_pk_bf16_f32 v147, v90, v91
	v_cvt_pk_bf16_f32 v128, v96, v97
	v_cvt_pk_bf16_f32 v129, v98, v99
	v_cvt_pk_bf16_f32 v130, v132, v133
	v_cvt_pk_bf16_f32 v131, v134, v135
	s_lshl_b32 s0, s2, 13
	s_cmp_lt_u32 s44, s42
	s_cselect_b32 s0, s0, 0x1e848000
	ds_read_b128 v[132:135], v115 offset:3072
	s_waitcnt lgkmcnt(3)
	v_mfma_f32_16x16x32_bf16 v[148:151], v[136:139], v[156:159], v[36:39]
	ds_read_b128 v[156:159], v115 offset:4096
	s_waitcnt lgkmcnt(3)
	v_mfma_f32_16x16x32_bf16 v[152:155], v[136:139], v[160:163], v[40:43]
	ds_read_b128 v[160:163], v115 offset:5120
	s_waitcnt lgkmcnt(3)
	v_mfma_f32_16x16x32_bf16 v[96:99], v[136:139], v[164:167], v[44:47]
	ds_read_b128 v[164:167], v115 offset:6144
	s_waitcnt lgkmcnt(3)
	v_mfma_f32_16x16x32_bf16 v[92:95], v[136:139], v[132:135], v[48:51]
	s_mov_b32 m0, s47
	s_nop 0
	buffer_load_dwordx4 v113, s[12:15], s0 offen nt lds
	ds_read_b128 v[132:135], v115 offset:7168
	s_waitcnt lgkmcnt(3)
	v_mfma_f32_16x16x32_bf16 v[88:91], v[136:139], v[156:159], v[52:55]
	ds_read_b128 v[156:159], v115 offset:8192
	s_waitcnt lgkmcnt(3)
	v_mfma_f32_16x16x32_bf16 v[84:87], v[136:139], v[160:163], v[56:59]
	ds_read_b128 v[160:163], v115 offset:9216
	s_waitcnt lgkmcnt(3)
	v_mfma_f32_16x16x32_bf16 v[80:83], v[136:139], v[164:167], v[60:63]
	ds_read_b128 v[164:167], v115 offset:10240
	s_waitcnt lgkmcnt(3)
	v_mfma_f32_16x16x32_bf16 v[76:79], v[136:139], v[132:135], v[64:67]
	s_or_b32 s1, s0, 0x100
	s_mov_b32 m0, s51
	s_nop 0
	buffer_load_dwordx4 v113, s[12:15], s1 offen nt lds
	ds_read_b128 v[132:135], v115 offset:11264
	s_waitcnt lgkmcnt(3)
	v_mfma_f32_16x16x32_bf16 v[148:151], v[140:143], v[156:159], v[148:151]
	ds_read_b128 v[156:159], v115 offset:12288
	s_waitcnt lgkmcnt(3)
	v_mfma_f32_16x16x32_bf16 v[152:155], v[140:143], v[160:163], v[152:155]
	ds_read_b128 v[160:163], v115 offset:13312
	s_waitcnt lgkmcnt(3)
	v_mfma_f32_16x16x32_bf16 v[96:99], v[140:143], v[164:167], v[96:99]
	ds_read_b128 v[164:167], v115 offset:14336
	s_waitcnt lgkmcnt(3)
	v_mfma_f32_16x16x32_bf16 v[92:95], v[140:143], v[132:135], v[92:95]
	s_or_b32 s1, s0, 0x800
	s_mov_b32 m0, s48
	s_nop 0
	buffer_load_dwordx4 v113, s[12:15], s1 offen nt lds
	ds_read_b128 v[132:135], v115 offset:15360
	s_waitcnt lgkmcnt(3)
	v_mfma_f32_16x16x32_bf16 v[88:91], v[140:143], v[156:159], v[88:91]
	ds_read_b128 v[156:159], v115 offset:16384
	s_waitcnt lgkmcnt(3)
	v_mfma_f32_16x16x32_bf16 v[84:87], v[140:143], v[160:163], v[84:87]
	ds_read_b128 v[160:163], v115 offset:17408
	s_waitcnt lgkmcnt(3)
	v_mfma_f32_16x16x32_bf16 v[80:83], v[140:143], v[164:167], v[80:83]
	ds_read_b128 v[164:167], v115 offset:18432
	s_waitcnt lgkmcnt(3)
	v_mfma_f32_16x16x32_bf16 v[76:79], v[140:143], v[132:135], v[76:79]
	s_or_b32 s1, s0, 0x900
	s_mov_b32 m0, s52
	s_nop 0
	buffer_load_dwordx4 v113, s[12:15], s1 offen nt lds
	ds_read_b128 v[132:135], v115 offset:19456
	s_waitcnt lgkmcnt(3)
	v_mfma_f32_16x16x32_bf16 v[148:151], v[144:147], v[156:159], v[148:151]
	ds_read_b128 v[156:159], v115 offset:20480
	s_waitcnt lgkmcnt(3)
	v_mfma_f32_16x16x32_bf16 v[152:155], v[144:147], v[160:163], v[152:155]
	ds_read_b128 v[160:163], v115 offset:21504
	s_waitcnt lgkmcnt(3)
	v_mfma_f32_16x16x32_bf16 v[96:99], v[144:147], v[164:167], v[96:99]
	ds_read_b128 v[164:167], v115 offset:22528
	s_waitcnt lgkmcnt(3)
	v_mfma_f32_16x16x32_bf16 v[92:95], v[144:147], v[132:135], v[92:95]
	s_or_b32 s1, s0, 0x1000
	s_mov_b32 m0, s49
	s_nop 0
	buffer_load_dwordx4 v113, s[12:15], s1 offen nt lds
	ds_read_b128 v[132:135], v115 offset:23552
	s_waitcnt lgkmcnt(3)
	v_mfma_f32_16x16x32_bf16 v[88:91], v[144:147], v[156:159], v[88:91]
	ds_read_b128 v[156:159], v115 offset:24576
	s_waitcnt lgkmcnt(3)
	v_mfma_f32_16x16x32_bf16 v[84:87], v[144:147], v[160:163], v[84:87]
	ds_read_b128 v[160:163], v115 offset:25600
	s_waitcnt lgkmcnt(3)
	v_mfma_f32_16x16x32_bf16 v[80:83], v[144:147], v[164:167], v[80:83]
	ds_read_b128 v[164:167], v115 offset:26624
	s_waitcnt lgkmcnt(3)
	v_mfma_f32_16x16x32_bf16 v[76:79], v[144:147], v[132:135], v[76:79]
	s_or_b32 s1, s0, 0x1100
	s_mov_b32 m0, s53
	s_nop 0
	buffer_load_dwordx4 v113, s[12:15], s1 offen nt lds
	ds_read_b128 v[132:135], v115 offset:27648
	s_waitcnt lgkmcnt(3)
	v_mfma_f32_16x16x32_bf16 v[148:151], v[128:131], v[156:159], v[148:151]
	ds_read_b128 v[156:159], v115 offset:28672
	s_waitcnt lgkmcnt(3)
	v_mfma_f32_16x16x32_bf16 v[152:155], v[128:131], v[160:163], v[152:155]
	ds_read_b128 v[160:163], v115 offset:29696
	s_waitcnt lgkmcnt(3)
	v_mfma_f32_16x16x32_bf16 v[96:99], v[128:131], v[164:167], v[96:99]
	ds_read_b128 v[164:167], v115 offset:30720
	s_waitcnt lgkmcnt(3)
	v_mfma_f32_16x16x32_bf16 v[92:95], v[128:131], v[132:135], v[92:95]
	s_or_b32 s1, s0, 0x1800
	s_mov_b32 m0, s50
	s_nop 0
	buffer_load_dwordx4 v113, s[12:15], s1 offen nt lds
	ds_read_b128 v[132:135], v115 offset:31744
	s_waitcnt lgkmcnt(3)
	v_mfma_f32_16x16x32_bf16 v[88:91], v[128:131], v[156:159], v[88:91]
	s_waitcnt lgkmcnt(2)
	v_mfma_f32_16x16x32_bf16 v[84:87], v[128:131], v[160:163], v[84:87]
	s_waitcnt lgkmcnt(1)
	v_mfma_f32_16x16x32_bf16 v[80:83], v[128:131], v[164:167], v[80:83]
	s_waitcnt lgkmcnt(0)
	v_mfma_f32_16x16x32_bf16 v[76:79], v[128:131], v[132:135], v[76:79]
	s_or_b32 s1, s0, 0x1900
	s_mov_b32 m0, s54
	s_nop 0
	buffer_load_dwordx4 v113, s[12:15], s1 offen nt lds
	ds_read2_b32 v[136:137], v114 offset0:128 offset1:144
	ds_read2_b32 v[138:139], v125 offset1:16
	ds_read2_b32 v[140:141], v114 offset0:160 offset1:176
	ds_read2_b32 v[142:143], v125 offset0:32 offset1:48
	ds_read2_b32 v[144:145], v114 offset0:192 offset1:208
	ds_read2_b32 v[146:147], v125 offset0:64 offset1:80
	ds_read2_b32 v[156:157], v114 offset0:224 offset1:240
	ds_read2_b32 v[158:159], v125 offset0:96 offset1:112
	v_fma_f32 v70, v149, v149, 0
	v_fmac_f32_e32 v70, v153, v153
	v_fmac_f32_e32 v70, v97, v97
	v_fmac_f32_e32 v70, v93, v93
	v_fmac_f32_e32 v70, v89, v89
	v_fmac_f32_e32 v70, v85, v85
	v_fmac_f32_e32 v70, v81, v81
	v_fmac_f32_e32 v70, v77, v77
	v_fma_f32 v68, v148, v148, 0
	v_fmac_f32_e32 v68, v152, v152
	v_add_f32_dpp v70, v70, v70 quad_perm:[1,0,3,2] row_mask:0xf bank_mask:0xf bound_ctrl:1
	v_fmac_f32_e32 v68, v96, v96
	v_fmac_f32_e32 v68, v92, v92
	v_add_f32_dpp v70, v70, v70 quad_perm:[2,3,0,1] row_mask:0xf bank_mask:0xf bound_ctrl:1
	v_fmac_f32_e32 v68, v88, v88
	v_fmac_f32_e32 v68, v84, v84
	v_add_f32_dpp v70, v70, v70 row_half_mirror row_mask:0xf bank_mask:0xf bound_ctrl:1
	v_fmac_f32_e32 v68, v80, v80
	v_fmac_f32_e32 v68, v76, v76
	v_add_f32_dpp v70, v70, v70 row_mirror row_mask:0xf bank_mask:0xf bound_ctrl:1
	v_fmamk_f32 v70, v70, 0x3c000000, v124
	v_rsq_f32_e32 v127, v70
	v_fma_f32 v70, v150, v150, 0
	v_fmac_f32_e32 v70, v154, v154
	v_fmac_f32_e32 v70, v98, v98
	v_fmac_f32_e32 v70, v94, v94
	v_fmac_f32_e32 v70, v90, v90
	v_fmac_f32_e32 v70, v86, v86
	v_fmac_f32_e32 v70, v82, v82
	v_fmac_f32_e32 v70, v78, v78
	v_add_f32_dpp v68, v68, v68 quad_perm:[1,0,3,2] row_mask:0xf bank_mask:0xf bound_ctrl:1
	v_mul_f32_e32 v131, v127, v149
	v_add_f32_dpp v70, v70, v70 quad_perm:[1,0,3,2] row_mask:0xf bank_mask:0xf bound_ctrl:1
	v_add_f32_dpp v68, v68, v68 quad_perm:[2,3,0,1] row_mask:0xf bank_mask:0xf bound_ctrl:1
	v_mul_f32_e32 v81, v127, v81
	v_add_f32_dpp v70, v70, v70 quad_perm:[2,3,0,1] row_mask:0xf bank_mask:0xf bound_ctrl:1
	v_add_f32_dpp v68, v68, v68 row_half_mirror row_mask:0xf bank_mask:0xf bound_ctrl:1
	v_cmp_gt_u32_e64 s[0:1], s55, v72
	v_add_f32_dpp v70, v70, v70 row_half_mirror row_mask:0xf bank_mask:0xf bound_ctrl:1
	v_add_f32_dpp v68, v68, v68 row_mirror row_mask:0xf bank_mask:0xf bound_ctrl:1
	v_fmamk_f32 v68, v68, 0x3c000000, v124
	v_add_f32_dpp v70, v70, v70 row_mirror row_mask:0xf bank_mask:0xf bound_ctrl:1
	v_fmamk_f32 v70, v70, 0x3c000000, v124
	v_rsq_f32_e32 v130, v70
	v_fma_f32 v70, v151, v151, 0
	v_fmac_f32_e32 v70, v155, v155
	v_fmac_f32_e32 v70, v99, v99
	v_fmac_f32_e32 v70, v95, v95
	v_fmac_f32_e32 v70, v91, v91
	v_fmac_f32_e32 v70, v87, v87
	v_fmac_f32_e32 v70, v83, v83
	v_fmac_f32_e32 v70, v79, v79
	v_rsq_f32_e32 v68, v68
	v_mul_f32_e32 v98, v130, v98
	v_add_f32_dpp v70, v70, v70 quad_perm:[1,0,3,2] row_mask:0xf bank_mask:0xf bound_ctrl:1
	v_mul_f32_e32 v90, v130, v90
	v_mul_f32_e32 v111, v68, v148
	v_add_f32_dpp v110, v70, v70 quad_perm:[2,3,0,1] row_mask:0xf bank_mask:0xf bound_ctrl:1
	s_nop 1
	v_add_f32_dpp v110, v110, v110 row_half_mirror row_mask:0xf bank_mask:0xf bound_ctrl:1
	v_mul_f32_e32 v96, v68, v96
	v_mul_f32_e32 v92, v68, v92
	v_add_f32_dpp v110, v110, v110 row_mirror row_mask:0xf bank_mask:0xf bound_ctrl:1
	v_fmamk_f32 v110, v110, 0x3c000000, v124
	s_waitcnt lgkmcnt(0)
	v_fma_f32 v111, v111, v136, v138
	v_fma_f32 v131, v131, v136, v138
	v_exp_f32_e32 v111, v111
	v_exp_f32_e32 v131, v131
	v_rsq_f32_e32 v132, v110
	v_mul_f32_e32 v88, v68, v88
	v_add_f32_e32 v110, 1.0, v111
	v_add_f32_e32 v111, 1.0, v131
	v_mul_f32_e32 v131, v130, v150
	v_mul_f32_e32 v133, v132, v151
	v_fma_f32 v131, v131, v136, v138
	v_fma_f32 v70, v133, v136, v138
	v_exp_f32_e32 v131, v131
	v_exp_f32_e32 v70, v70
	v_rcp_f32_e32 v110, v110
	v_rcp_f32_e32 v111, v111
	v_add_f32_e32 v128, 1.0, v131
	v_add_f32_e32 v70, 1.0, v70
	v_rcp_f32_e32 v128, v128
	v_rcp_f32_e32 v70, v70
	v_mul_f32_e32 v131, v68, v152
	v_fma_f32 v131, v131, v137, v139
	v_cvt_pk_bf16_f32 v110, v110, v111
	v_cvt_pk_bf16_f32 v111, v128, v70
	v_mul_f32_e32 v128, v127, v153
	v_exp_f32_e32 v131, v131
	v_fma_f32 v128, v128, v137, v139
	v_exp_f32_e32 v128, v128
	v_mul_f32_e32 v99, v132, v99
	v_add_f32_e32 v70, 1.0, v131
	v_rcp_f32_e32 v133, v70
	v_add_f32_e32 v70, 1.0, v128
	v_mul_f32_e32 v131, v130, v154
	v_rcp_f32_e32 v134, v70
	v_mul_f32_e32 v70, v132, v155
	v_fma_f32 v131, v131, v137, v139
	v_fma_f32 v129, v70, v137, v139
	v_exp_f32_e32 v135, v129
	v_exp_f32_e32 v131, v131
	v_mul_f32_e32 v91, v132, v91
	v_add_f32_e32 v135, 1.0, v135
	v_rcp_f32_e32 v135, v135
	v_fma_f32 v96, v96, v140, v142
	v_exp_f32_e32 v136, v96
	v_mul_f32_e32 v96, v127, v97
	v_fma_f32 v96, v96, v140, v142
	v_exp_f32_e32 v97, v96
	v_fma_f32 v98, v98, v140, v142
	v_fma_f32 v70, v99, v140, v142
	v_exp_f32_e32 v98, v98
	v_exp_f32_e32 v70, v70
	v_add_f32_e32 v97, 1.0, v97
	v_cvt_pk_bf16_f32 v96, v133, v134
	v_add_f32_e32 v133, 1.0, v136
	v_rcp_f32_e32 v99, v97
	v_add_f32_e32 v97, 1.0, v98
	v_add_f32_e32 v70, 1.0, v70
	v_fma_f32 v92, v92, v141, v143
	v_rcp_f32_e32 v133, v133
	v_rcp_f32_e32 v128, v97
	v_rcp_f32_e32 v70, v70
	v_exp_f32_e32 v92, v92
	v_cvt_pk_bf16_f32 v98, v133, v99
	v_add_f32_e32 v131, 1.0, v131
	v_cvt_pk_bf16_f32 v99, v128, v70
	v_add_f32_e32 v70, 1.0, v92
	v_mul_f32_e32 v92, v127, v93
	v_fma_f32 v92, v92, v141, v143
	v_exp_f32_e32 v92, v92
	v_mul_f32_e32 v93, v130, v94
	v_fma_f32 v93, v93, v141, v143
	v_rcp_f32_e32 v131, v131
	v_exp_f32_e32 v93, v93
	v_rcp_f32_e32 v94, v70
	v_add_f32_e32 v70, 1.0, v92
	v_rcp_f32_e32 v128, v70
	v_mul_f32_e32 v70, v132, v95
	v_cvt_pk_bf16_f32 v97, v131, v135
	v_add_f32_e32 v131, 1.0, v93
	v_fma_f32 v129, v70, v141, v143
	v_exp_f32_e32 v95, v129
	v_rcp_f32_e32 v129, v131
	v_mul_f32_e32 v84, v68, v84
	v_mul_f32_e32 v80, v68, v80
	v_fma_f32 v88, v88, v144, v146
	v_exp_f32_e32 v131, v88
	v_mul_f32_e32 v88, v127, v89
	v_fma_f32 v88, v88, v144, v146
	v_exp_f32_e32 v89, v88
	v_fma_f32 v90, v90, v144, v146
	v_fma_f32 v70, v91, v144, v146
	v_exp_f32_e32 v90, v90
	v_exp_f32_e32 v70, v70
	v_add_f32_e32 v89, 1.0, v89
	v_cvt_pk_bf16_f32 v88, v94, v128
	v_add_f32_e32 v94, 1.0, v131
	v_rcp_f32_e32 v91, v89
	v_add_f32_e32 v89, 1.0, v90
	v_add_f32_e32 v70, 1.0, v70
	v_fma_f32 v84, v84, v145, v147
	v_rcp_f32_e32 v94, v94
	v_rcp_f32_e32 v92, v89
	v_rcp_f32_e32 v70, v70
	v_exp_f32_e32 v84, v84
	v_cvt_pk_bf16_f32 v90, v94, v91
	v_mul_f32_e32 v68, v68, v76
	v_cvt_pk_bf16_f32 v91, v92, v70
	v_add_f32_e32 v70, 1.0, v84
	v_mul_f32_e32 v84, v127, v85
	v_fma_f32 v84, v84, v145, v147
	v_mul_f32_e32 v85, v130, v86
	v_exp_f32_e32 v84, v84
	v_fma_f32 v85, v85, v145, v147
	v_exp_f32_e32 v85, v85
	v_rcp_f32_e32 v92, v70
	v_add_f32_e32 v70, 1.0, v84
	v_rcp_f32_e32 v84, v70
	v_add_f32_e32 v70, 1.0, v85
	v_mul_f32_e32 v85, v132, v87
	v_fma_f32 v93, v85, v145, v147
	v_exp_f32_e32 v85, v93
	v_rcp_f32_e32 v93, v70
	v_mul_f32_e32 v76, v127, v77
	v_mul_f32_e32 v82, v130, v82
	v_mul_f32_e32 v83, v132, v83
	v_mul_f32_e32 v77, v130, v78
	v_fma_f32 v76, v76, v157, v159
	v_mul_f32_e32 v78, v132, v79
	v_fma_f32 v80, v80, v156, v158
	v_fma_f32 v81, v81, v156, v158
	v_fma_f32 v82, v82, v156, v158
	v_fma_f32 v70, v83, v156, v158
	v_fma_f32 v68, v68, v157, v159
	v_exp_f32_e32 v76, v76
	v_fma_f32 v77, v77, v157, v159
	v_fma_f32 v87, v78, v157, v159
	v_exp_f32_e32 v82, v82
	v_exp_f32_e32 v70, v70
	v_exp_f32_e32 v68, v68
	v_exp_f32_e32 v77, v77
	v_exp_f32_e32 v71, v87
	v_add_f32_e32 v76, 1.0, v76
	v_add_f32_e32 v82, 1.0, v82
	v_add_f32_e32 v70, 1.0, v70
	v_add_f32_e32 v68, 1.0, v68
	v_rcp_f32_e32 v78, v76
	v_add_f32_e32 v76, 1.0, v77
	v_add_f32_e32 v71, 1.0, v71
	v_rcp_f32_e32 v82, v82
	v_rcp_f32_e32 v70, v70
	v_rcp_f32_e32 v68, v68
	v_rcp_f32_e32 v79, v76
	v_rcp_f32_e32 v71, v71
	v_exp_f32_e32 v80, v80
	v_exp_f32_e32 v81, v81
	v_cvt_pk_bf16_f32 v77, v82, v70
	v_cvt_pk_bf16_f32 v78, v68, v78
	v_cvt_pk_bf16_f32 v79, v79, v71
	v_subrev_u32_e32 v68, s16, v72
	v_subrev_u32_e32 v70, s16, v73
	v_subrev_u32_e32 v71, s16, v74
	v_add_f32_e32 v95, 1.0, v95
	v_add_f32_e32 v85, 1.0, v85
	v_add_f32_e32 v80, 1.0, v80
	v_add_f32_e32 v81, 1.0, v81
	v_max3_u32 v68, v68, v70, v71
	v_subrev_u32_e32 v70, s16, v75
	v_rcp_f32_e32 v95, v95
	v_rcp_f32_e32 v85, v85
	v_rcp_f32_e32 v80, v80
	v_rcp_f32_e32 v81, v81
	v_max_u32_e32 v68, v68, v70
	v_cmp_gt_u32_e32 vcc, 16, v68
	s_cmp_eq_u64 vcc, -1
	s_cselect_b64 s[24:25], -1, 0
	s_cmp_lg_u64 vcc, -1
	v_cvt_pk_bf16_f32 v89, v129, v95
	v_cvt_pk_bf16_f32 v84, v92, v84
	v_cvt_pk_bf16_f32 v85, v93, v85
	v_cvt_pk_bf16_f32 v76, v80, v81
	s_cselect_b64 s[26:27], -1, 0
	v_cmp_gt_u32_e64 s[2:3], s55, v73
	v_cmp_gt_u32_e64 s[4:5], s55, v74
	v_cmp_gt_u32_e64 s[6:7], s55, v75
	s_mov_b32 s8, 0
	s_branch .LBB1_14
